# coalesced output stores made write-through (sc0 sc1) so no dirty L2 flush at kernel end
# baseline (speedup 1.0000x reference)
.LBB2_369:
	v_xor_b32_e32 v0, 1, v51
	v_add_u32_e32 v1, 64, v52
	v_cmp_lt_i32_e32 vcc, v0, v1
	s_waitcnt lgkmcnt(0)
	v_mul_f32_e32 v2, v53, v2
	v_cndmask_b32_e32 v0, v51, v0, vcc
	v_lshlrev_b32_e32 v65, 2, v0
	v_mul_f32_e32 v0, v53, v6
	s_nop 1
	v_mov_b32_dpp v1, v0 quad_perm:[1,0,3,2] row_mask:0xf bank_mask:0xf
	v_cmp_eq_u32_e32 vcc, 0, v44
	v_mul_f32_e32 v6, v53, v7
	s_nop 1
	v_mov_b32_dpp v7, v6 quad_perm:[1,0,3,2] row_mask:0xf bank_mask:0xf
	s_waitcnt lgkmcnt(1)
	v_cndmask_b32_e32 v52, v1, v0, vcc
	v_cndmask_b32_e32 v70, v0, v1, vcc
	v_mul_f32_e32 v0, v53, v8
	s_nop 1
	v_mov_b32_dpp v1, v0 quad_perm:[1,0,3,2] row_mask:0xf bank_mask:0xf
	s_nop 1
	v_mov_b32_dpp v8, v2 quad_perm:[1,0,3,2] row_mask:0xf bank_mask:0xf
	s_waitcnt lgkmcnt(2)
	v_cndmask_b32_e32 v54, v7, v6, vcc
	v_cndmask_b32_e32 v68, v6, v7, vcc
	v_mul_f32_e32 v6, v53, v9
	s_waitcnt lgkmcnt(1)
	v_cndmask_b32_e32 v56, v1, v0, vcc
	v_cndmask_b32_e32 v76, v0, v1, vcc
	v_mul_f32_e32 v0, v53, v3
	s_nop 1
	v_mov_b32_dpp v1, v0 quad_perm:[1,0,3,2] row_mask:0xf bank_mask:0xf
	s_waitcnt lgkmcnt(1)
	v_cndmask_b32_e32 v60, v8, v2, vcc
	v_cndmask_b32_e32 v72, v2, v8, vcc
	v_mul_f32_e32 v2, v53, v4
	v_mul_f32_e32 v4, v53, v5
	s_nop 1
	v_mov_b32_dpp v5, v4 quad_perm:[1,0,3,2] row_mask:0xf bank_mask:0xf
	s_nop 1
	v_mov_b32_dpp v3, v2 quad_perm:[1,0,3,2] row_mask:0xf bank_mask:0xf
	s_nop 1
	v_mov_b32_dpp v7, v6 quad_perm:[1,0,3,2] row_mask:0xf bank_mask:0xf
	s_waitcnt lgkmcnt(3)
	v_cndmask_b32_e32 v62, v1, v0, vcc
	v_cndmask_b32_e32 v82, v0, v1, vcc
	v_mul_u32_u24_e32 v0, 20, v44
	v_lshlrev_b32_e32 v66, 2, v0
	s_waitcnt lgkmcnt(2)
	v_cndmask_b32_e32 v84, v5, v4, vcc
	v_cndmask_b32_e32 v78, v4, v5, vcc
	v_add_u32_e32 v66, 0x16400, v66
	s_waitcnt lgkmcnt(1)
	v_cndmask_b32_e32 v86, v3, v2, vcc
	v_cndmask_b32_e32 v80, v2, v3, vcc
	ds_read_b128 v[48:51], v66 offset:6224
	ds_read_b128 v[88:91], v66 offset:6240
	ds_read_b128 v[32:35], v66 offset:6256
	ds_read_b128 v[16:19], v66 offset:6272
	ds_read_b128 v[0:3], v66 offset:6288
	ds_read_b128 v[92:95], v66
	ds_read_b128 v[96:99], v66 offset:16
	ds_read_b128 v[40:43], v66 offset:32
	s_waitcnt lgkmcnt(8)
	v_cndmask_b32_e32 v58, v7, v6, vcc
	v_cndmask_b32_e32 v74, v6, v7, vcc
	ds_read_b128 v[20:23], v66 offset:48
	ds_read_b128 v[4:7], v66 offset:64
	ds_read_b128 v[100:103], v66 offset:160
	ds_read_b128 v[104:107], v66 offset:176
	ds_read_b128 v[36:39], v66 offset:192
	ds_read_b128 v[24:27], v66 offset:208
	s_waitcnt vmcnt(0)
	ds_read_b128 v[8:11], v66 offset:224
	ds_read_b128 v[108:111], v66 offset:320
	ds_read_b128 v[112:115], v66 offset:336
	ds_read_b128 v[44:47], v66 offset:352
	ds_read_b128 v[28:31], v66 offset:368
	ds_read_b128 v[12:15], v66 offset:384
	s_waitcnt lgkmcnt(14)
	v_pk_fma_f32 v[48:49], v[52:53], v[92:93], v[48:49] op_sel_hi:[0,1,1]
	v_pk_fma_f32 v[50:51], v[52:53], v[94:95], v[50:51] op_sel_hi:[0,1,1]
	ds_read_b128 v[92:95], v66 offset:480
	ds_read_b128 v[116:119], v66 offset:496
	s_waitcnt lgkmcnt(11)
	v_pk_fma_f32 v[48:49], v[54:55], v[100:101], v[48:49] op_sel_hi:[0,1,1]
	v_pk_fma_f32 v[50:51], v[54:55], v[102:103], v[50:51] op_sel_hi:[0,1,1]
	ds_read_b128 v[120:123], v66 offset:512
	ds_read_b128 v[124:127], v66 offset:528
	s_waitcnt lgkmcnt(8)
	v_pk_fma_f32 v[100:101], v[56:57], v[108:109], v[48:49] op_sel_hi:[0,1,1]
	v_pk_fma_f32 v[102:103], v[56:57], v[110:111], v[50:51] op_sel_hi:[0,1,1]
	v_pk_fma_f32 v[96:97], v[52:53], v[96:97], v[88:89] op_sel_hi:[0,1,1]
	v_pk_fma_f32 v[108:109], v[52:53], v[98:99], v[90:91] op_sel_hi:[0,1,1]
	ds_read_b128 v[48:51], v66 offset:544
	ds_read_b128 v[88:91], v66 offset:640
	s_waitcnt lgkmcnt(5)
	v_pk_fma_f32 v[98:99], v[58:59], v[92:93], v[100:101] op_sel_hi:[0,1,1]
	v_pk_fma_f32 v[100:101], v[58:59], v[94:95], v[102:103] op_sel_hi:[0,1,1]
	ds_read_b128 v[92:95], v66 offset:800
	s_waitcnt lgkmcnt(1)
	v_pk_fma_f32 v[98:99], v[60:61], v[88:89], v[98:99] op_sel_hi:[0,1,1]
	v_pk_fma_f32 v[100:101], v[60:61], v[90:91], v[100:101] op_sel_hi:[0,1,1]
	ds_read_b128 v[88:91], v66 offset:816
	s_waitcnt lgkmcnt(1)
	v_pk_fma_f32 v[98:99], v[62:63], v[92:93], v[98:99] op_sel_hi:[0,1,1]
	v_pk_fma_f32 v[92:93], v[62:63], v[94:95], v[100:101] op_sel_hi:[0,1,1]
	v_pk_fma_f32 v[100:101], v[54:55], v[104:105], v[96:97] op_sel_hi:[0,1,1]
	v_pk_fma_f32 v[102:103], v[54:55], v[106:107], v[108:109] op_sel_hi:[0,1,1]
	ds_read_b128 v[94:97], v66 offset:656
	ds_read_b128 v[108:111], v66 offset:672
	v_pk_fma_f32 v[100:101], v[56:57], v[112:113], v[100:101] op_sel_hi:[0,1,1]
	v_pk_fma_f32 v[102:103], v[56:57], v[114:115], v[102:103] op_sel_hi:[0,1,1]
	v_pk_fma_f32 v[100:101], v[58:59], v[116:117], v[100:101] op_sel_hi:[0,1,1]
	v_pk_fma_f32 v[102:103], v[58:59], v[118:119], v[102:103] op_sel_hi:[0,1,1]
	ds_read_b128 v[112:115], v66 offset:688
	ds_read_b128 v[116:119], v66 offset:704
	v_pk_fma_f32 v[32:33], v[52:53], v[40:41], v[32:33] op_sel_hi:[0,1,1]
	v_pk_fma_f32 v[32:33], v[54:55], v[36:37], v[32:33] op_sel_hi:[0,1,1]
	v_pk_fma_f32 v[32:33], v[56:57], v[44:45], v[32:33] op_sel_hi:[0,1,1]
	s_waitcnt lgkmcnt(3)
	v_pk_fma_f32 v[94:95], v[60:61], v[94:95], v[100:101] op_sel_hi:[0,1,1]
	v_pk_fma_f32 v[32:33], v[58:59], v[120:121], v[32:33] op_sel_hi:[0,1,1]
	v_pk_fma_f32 v[106:107], v[62:63], v[88:89], v[94:95] op_sel_hi:[0,1,1]
	v_pk_fma_f32 v[88:89], v[60:61], v[96:97], v[102:103] op_sel_hi:[0,1,1]
	s_waitcnt lgkmcnt(2)
	v_pk_fma_f32 v[36:37], v[60:61], v[108:109], v[32:33] op_sel_hi:[0,1,1]
	v_pk_fma_f32 v[104:105], v[62:63], v[90:91], v[88:89] op_sel_hi:[0,1,1]
	ds_read_b128 v[88:91], v66 offset:832
	v_pk_fma_f32 v[40:41], v[52:53], v[42:43], v[34:35] op_sel_hi:[0,1,1]
	ds_read_b128 v[32:35], v66 offset:848
	v_pk_fma_f32 v[16:17], v[52:53], v[20:21], v[16:17] op_sel_hi:[0,1,1]
	v_pk_fma_f32 v[16:17], v[54:55], v[24:25], v[16:17] op_sel_hi:[0,1,1]
	v_pk_fma_f32 v[16:17], v[56:57], v[28:29], v[16:17] op_sel_hi:[0,1,1]
	v_pk_fma_f32 v[16:17], v[58:59], v[124:125], v[16:17] op_sel_hi:[0,1,1]
	s_waitcnt lgkmcnt(3)
	v_pk_fma_f32 v[16:17], v[60:61], v[112:113], v[16:17] op_sel_hi:[0,1,1]
	s_waitcnt lgkmcnt(1)
	v_pk_fma_f32 v[102:103], v[62:63], v[88:89], v[36:37] op_sel_hi:[0,1,1]
	s_waitcnt lgkmcnt(0)
	v_pk_fma_f32 v[88:89], v[62:63], v[32:33], v[16:17] op_sel_hi:[0,1,1]
	v_pk_fma_f32 v[16:17], v[52:53], v[22:23], v[18:19] op_sel_hi:[0,1,1]
	v_pk_fma_f32 v[16:17], v[54:55], v[26:27], v[16:17] op_sel_hi:[0,1,1]
	v_pk_fma_f32 v[16:17], v[56:57], v[30:31], v[16:17] op_sel_hi:[0,1,1]
	v_pk_fma_f32 v[16:17], v[58:59], v[126:127], v[16:17] op_sel_hi:[0,1,1]
	v_pk_fma_f32 v[16:17], v[60:61], v[114:115], v[16:17] op_sel_hi:[0,1,1]
	v_pk_fma_f32 v[94:95], v[62:63], v[34:35], v[16:17] op_sel_hi:[0,1,1]
	ds_read_b128 v[16:19], v66 offset:864
	v_pk_fma_f32 v[0:1], v[52:53], v[4:5], v[0:1] op_sel_hi:[0,1,1]
	v_pk_fma_f32 v[0:1], v[54:55], v[8:9], v[0:1] op_sel_hi:[0,1,1]
	v_pk_fma_f32 v[0:1], v[56:57], v[12:13], v[0:1] op_sel_hi:[0,1,1]
	v_pk_fma_f32 v[0:1], v[58:59], v[48:49], v[0:1] op_sel_hi:[0,1,1]
	v_pk_fma_f32 v[0:1], v[60:61], v[116:117], v[0:1] op_sel_hi:[0,1,1]
	ds_read_b128 v[32:35], v66 offset:960
	s_waitcnt lgkmcnt(1)
	v_pk_fma_f32 v[96:97], v[62:63], v[16:17], v[0:1] op_sel_hi:[0,1,1]
	v_pk_fma_f32 v[0:1], v[52:53], v[6:7], v[2:3] op_sel_hi:[0,1,1]
	v_pk_fma_f32 v[36:37], v[54:55], v[38:39], v[40:41] op_sel_hi:[0,1,1]
	v_pk_fma_f32 v[0:1], v[54:55], v[10:11], v[0:1] op_sel_hi:[0,1,1]
	v_pk_fma_f32 v[36:37], v[56:57], v[46:47], v[36:37] op_sel_hi:[0,1,1]
	v_pk_fma_f32 v[0:1], v[56:57], v[14:15], v[0:1] op_sel_hi:[0,1,1]
	v_pk_fma_f32 v[36:37], v[58:59], v[122:123], v[36:37] op_sel_hi:[0,1,1]
	v_pk_fma_f32 v[0:1], v[58:59], v[50:51], v[0:1] op_sel_hi:[0,1,1]
	v_pk_fma_f32 v[36:37], v[60:61], v[110:111], v[36:37] op_sel_hi:[0,1,1]
	v_pk_fma_f32 v[0:1], v[60:61], v[118:119], v[0:1] op_sel_hi:[0,1,1]
	v_pk_fma_f32 v[100:101], v[62:63], v[90:91], v[36:37] op_sel_hi:[0,1,1]
	v_pk_fma_f32 v[90:91], v[62:63], v[18:19], v[0:1] op_sel_hi:[0,1,1]
	ds_read_b128 v[48:51], v66 offset:976
	ds_read_b128 v[28:31], v66 offset:992
	ds_read_b128 v[16:19], v66 offset:1008
	ds_read_b128 v[0:3], v66 offset:1024
	ds_read_b128 v[44:47], v66 offset:1120
	ds_read_b128 v[52:55], v66 offset:1136
	ds_read_b128 v[36:39], v66 offset:1152
	ds_read_b128 v[20:23], v66 offset:1168
	ds_read_b128 v[4:7], v66 offset:1184
	ds_read_b128 v[108:111], v66 offset:1280
	ds_read_b128 v[56:59], v66 offset:1296
	ds_read_b128 v[40:43], v66 offset:1312
	ds_read_b128 v[24:27], v66 offset:1328
	ds_read_b128 v[8:11], v66 offset:1344
	ds_read_b128 v[112:115], v66 offset:1440
	ds_read_b128 v[60:63], v66 offset:1456
	ds_read_b128 v[12:15], v66 offset:1504
	ds_read_b128 v[116:119], v66 offset:1600
	s_waitcnt lgkmcnt(14)
	v_pk_fma_f32 v[32:33], v[86:87], v[32:33], v[98:99] op_sel_hi:[0,1,1]
	v_pk_fma_f32 v[34:35], v[86:87], v[34:35], v[92:93] op_sel_hi:[0,1,1]
	s_waitcnt lgkmcnt(13)
	v_pk_fma_f32 v[32:33], v[84:85], v[44:45], v[32:33] op_sel_hi:[0,1,1]
	v_pk_fma_f32 v[34:35], v[84:85], v[46:47], v[34:35] op_sel_hi:[0,1,1]
	ds_read_b128 v[120:123], v66 offset:1760
	ds_read_b128 v[124:127], v66 offset:1776
	s_waitcnt lgkmcnt(10)
	v_pk_fma_f32 v[92:93], v[70:71], v[108:109], v[32:33] op_sel_hi:[0,1,1]
	v_pk_fma_f32 v[98:99], v[70:71], v[110:111], v[34:35] op_sel_hi:[0,1,1]
	ds_read_b128 v[32:35], v66 offset:1824
	ds_read_b128 v[44:47], v66 offset:1920
	s_waitcnt lgkmcnt(7)
	v_pk_fma_f32 v[92:93], v[68:69], v[112:113], v[92:93] op_sel_hi:[0,1,1]
	v_pk_fma_f32 v[98:99], v[68:69], v[114:115], v[98:99] op_sel_hi:[0,1,1]
	ds_read_b128 v[108:111], v66 offset:2080
	ds_read_b128 v[112:115], v66 offset:2096
	s_waitcnt lgkmcnt(6)
	v_pk_fma_f32 v[92:93], v[76:77], v[116:117], v[92:93] op_sel_hi:[0,1,1]
	v_pk_fma_f32 v[98:99], v[76:77], v[118:119], v[98:99] op_sel_hi:[0,1,1]
	s_waitcnt lgkmcnt(5)
	v_pk_fma_f32 v[92:93], v[74:75], v[120:121], v[92:93] op_sel_hi:[0,1,1]
	v_pk_fma_f32 v[98:99], v[74:75], v[122:123], v[98:99] op_sel_hi:[0,1,1]
	s_waitcnt lgkmcnt(2)
	v_pk_fma_f32 v[92:93], v[72:73], v[44:45], v[92:93] op_sel_hi:[0,1,1]
	v_pk_fma_f32 v[98:99], v[72:73], v[46:47], v[98:99] op_sel_hi:[0,1,1]
	ds_read_b128 v[44:47], v66 offset:2144
	ds_read_b128 v[116:119], v66 offset:2240
	s_waitcnt lgkmcnt(3)
	v_pk_fma_f32 v[92:93], v[82:83], v[108:109], v[92:93] op_sel_hi:[0,1,1]
	v_pk_fma_f32 v[98:99], v[82:83], v[110:111], v[98:99] op_sel_hi:[0,1,1]
	ds_read_b128 v[108:111], v66 offset:2400
	s_waitcnt lgkmcnt(1)
	v_pk_fma_f32 v[92:93], v[80:81], v[116:117], v[92:93] op_sel_hi:[0,1,1]
	v_pk_fma_f32 v[98:99], v[80:81], v[118:119], v[98:99] op_sel_hi:[0,1,1]
	s_waitcnt lgkmcnt(0)
	v_pk_fma_f32 v[92:93], v[78:79], v[108:109], v[92:93] op_sel_hi:[0,1,1]
	v_pk_fma_f32 v[98:99], v[78:79], v[110:111], v[98:99] op_sel_hi:[0,1,1]
	v_pk_fma_f32 v[108:109], v[86:87], v[48:49], v[106:107] op_sel_hi:[0,1,1]
	v_pk_fma_f32 v[110:111], v[86:87], v[50:51], v[104:105] op_sel_hi:[0,1,1]
	ds_read_b128 v[116:119], v66 offset:2416
	ds_read_b128 v[104:107], v66 offset:1472
	ds_read_b128 v[48:51], v66 offset:1488
	v_pk_fma_f32 v[52:53], v[84:85], v[52:53], v[108:109] op_sel_hi:[0,1,1]
	v_pk_fma_f32 v[54:55], v[84:85], v[54:55], v[110:111] op_sel_hi:[0,1,1]
	v_pk_fma_f32 v[56:57], v[70:71], v[56:57], v[52:53] op_sel_hi:[0,1,1]
	v_pk_fma_f32 v[58:59], v[70:71], v[58:59], v[54:55] op_sel_hi:[0,1,1]
	ds_read_b128 v[52:55], v66 offset:1616
	ds_read_b128 v[108:111], v66 offset:1632
	v_pk_fma_f32 v[56:57], v[68:69], v[60:61], v[56:57] op_sel_hi:[0,1,1]
	v_pk_fma_f32 v[58:59], v[68:69], v[62:63], v[58:59] op_sel_hi:[0,1,1]
	s_waitcnt lgkmcnt(1)
	v_pk_fma_f32 v[56:57], v[76:77], v[52:53], v[56:57] op_sel_hi:[0,1,1]
	v_pk_fma_f32 v[58:59], v[76:77], v[54:55], v[58:59] op_sel_hi:[0,1,1]
	ds_read_b128 v[52:55], v66 offset:1936
	v_pk_fma_f32 v[56:57], v[74:75], v[124:125], v[56:57] op_sel_hi:[0,1,1]
	v_pk_fma_f32 v[58:59], v[74:75], v[126:127], v[58:59] op_sel_hi:[0,1,1]
	ds_read_b128 v[60:63], v66 offset:1952
	s_waitcnt lgkmcnt(1)
	v_pk_fma_f32 v[56:57], v[72:73], v[52:53], v[56:57] op_sel_hi:[0,1,1]
	v_pk_fma_f32 v[58:59], v[72:73], v[54:55], v[58:59] op_sel_hi:[0,1,1]
	ds_read_b128 v[52:55], v66 offset:2256
	v_pk_fma_f32 v[56:57], v[82:83], v[112:113], v[56:57] op_sel_hi:[0,1,1]
	v_pk_fma_f32 v[58:59], v[82:83], v[114:115], v[58:59] op_sel_hi:[0,1,1]
	s_waitcnt lgkmcnt(0)
	v_pk_fma_f32 v[56:57], v[80:81], v[52:53], v[56:57] op_sel_hi:[0,1,1]
	v_pk_fma_f32 v[58:59], v[80:81], v[54:55], v[58:59] op_sel_hi:[0,1,1]
	v_pk_fma_f32 v[56:57], v[78:79], v[116:117], v[56:57] op_sel_hi:[0,1,1]
	v_pk_fma_f32 v[58:59], v[78:79], v[118:119], v[58:59] op_sel_hi:[0,1,1]
	v_pk_fma_f32 v[116:117], v[86:87], v[28:29], v[102:103] op_sel_hi:[0,1,1]
	v_pk_fma_f32 v[118:119], v[86:87], v[30:31], v[100:101] op_sel_hi:[0,1,1]
	ds_read_b128 v[112:115], v66 offset:2272
	ds_read_b128 v[120:123], v66 offset:1648
	ds_read_b128 v[52:55], v66 offset:1664
	v_pk_fma_f32 v[36:37], v[84:85], v[36:37], v[116:117] op_sel_hi:[0,1,1]
	v_pk_fma_f32 v[38:39], v[84:85], v[38:39], v[118:119] op_sel_hi:[0,1,1]
	ds_read_b128 v[28:31], v66 offset:1792
	ds_read_b128 v[100:103], v66 offset:1808
	v_pk_fma_f32 v[116:117], v[70:71], v[40:41], v[36:37] op_sel_hi:[0,1,1]
	v_pk_fma_f32 v[118:119], v[70:71], v[42:43], v[38:39] op_sel_hi:[0,1,1]
	ds_read_b128 v[36:39], v66 offset:1968
	ds_read_b128 v[40:43], v66 offset:1984
	v_pk_fma_f32 v[104:105], v[68:69], v[104:105], v[116:117] op_sel_hi:[0,1,1]
	v_pk_fma_f32 v[106:107], v[68:69], v[106:107], v[118:119] op_sel_hi:[0,1,1]
	v_pk_fma_f32 v[116:117], v[76:77], v[108:109], v[104:105] op_sel_hi:[0,1,1]
	v_pk_fma_f32 v[118:119], v[76:77], v[110:111], v[106:107] op_sel_hi:[0,1,1]
	ds_read_b128 v[104:107], v66 offset:2112
	ds_read_b128 v[108:111], v66 offset:2128
	s_waitcnt lgkmcnt(5)
	v_pk_fma_f32 v[28:29], v[74:75], v[28:29], v[116:117] op_sel_hi:[0,1,1]
	v_pk_fma_f32 v[30:31], v[74:75], v[30:31], v[118:119] op_sel_hi:[0,1,1]
	v_pk_fma_f32 v[16:17], v[86:87], v[16:17], v[88:89] op_sel_hi:[0,1,1]
	v_pk_fma_f32 v[28:29], v[72:73], v[60:61], v[28:29] op_sel_hi:[0,1,1]
	v_pk_fma_f32 v[30:31], v[72:73], v[62:63], v[30:31] op_sel_hi:[0,1,1]
	ds_read_b128 v[60:63], v66 offset:2288
	ds_read_b128 v[116:119], v66 offset:2304
	v_pk_fma_f32 v[16:17], v[84:85], v[20:21], v[16:17] op_sel_hi:[0,1,1]
	v_pk_fma_f32 v[18:19], v[86:87], v[18:19], v[94:95] op_sel_hi:[0,1,1]
	s_waitcnt lgkmcnt(3)
	v_pk_fma_f32 v[104:105], v[82:83], v[104:105], v[28:29] op_sel_hi:[0,1,1]
	v_pk_fma_f32 v[106:107], v[82:83], v[106:107], v[30:31] op_sel_hi:[0,1,1]
	ds_read_b128 v[28:31], v66 offset:2432
	v_pk_fma_f32 v[16:17], v[70:71], v[24:25], v[16:17] op_sel_hi:[0,1,1]
	v_pk_fma_f32 v[18:19], v[84:85], v[22:23], v[18:19] op_sel_hi:[0,1,1]
	v_pk_fma_f32 v[0:1], v[86:87], v[0:1], v[96:97] op_sel_hi:[0,1,1]
	v_pk_fma_f32 v[16:17], v[68:69], v[48:49], v[16:17] op_sel_hi:[0,1,1]
	v_pk_fma_f32 v[18:19], v[70:71], v[26:27], v[18:19] op_sel_hi:[0,1,1]
	ds_read_b128 v[20:23], v66 offset:2464
	v_pk_fma_f32 v[0:1], v[84:85], v[4:5], v[0:1] op_sel_hi:[0,1,1]
	v_pk_fma_f32 v[2:3], v[86:87], v[2:3], v[90:91] op_sel_hi:[0,1,1]
	v_pk_fma_f32 v[112:113], v[80:81], v[112:113], v[104:105] op_sel_hi:[0,1,1]
	v_pk_fma_f32 v[114:115], v[80:81], v[114:115], v[106:107] op_sel_hi:[0,1,1]
	ds_read_b128 v[104:107], v66 offset:2448
	v_subrev_u32_e32 v66, 0x16400, v66
	v_pk_fma_f32 v[16:17], v[76:77], v[120:121], v[16:17] op_sel_hi:[0,1,1]
	v_pk_fma_f32 v[18:19], v[68:69], v[50:51], v[18:19] op_sel_hi:[0,1,1]
	v_pk_fma_f32 v[0:1], v[70:71], v[8:9], v[0:1] op_sel_hi:[0,1,1]
	v_pk_fma_f32 v[2:3], v[84:85], v[6:7], v[2:3] op_sel_hi:[0,1,1]
	v_max_f32_e32 v4, v92, v93
	v_pk_fma_f32 v[16:17], v[74:75], v[100:101], v[16:17] op_sel_hi:[0,1,1]
	v_pk_fma_f32 v[18:19], v[76:77], v[122:123], v[18:19] op_sel_hi:[0,1,1]
	v_pk_fma_f32 v[0:1], v[68:69], v[12:13], v[0:1] op_sel_hi:[0,1,1]
	v_pk_fma_f32 v[2:3], v[70:71], v[10:11], v[2:3] op_sel_hi:[0,1,1]
	v_max3_f32 v4, v4, v98, v99
	v_pk_fma_f32 v[16:17], v[72:73], v[36:37], v[16:17] op_sel_hi:[0,1,1]
	v_pk_fma_f32 v[18:19], v[74:75], v[102:103], v[18:19] op_sel_hi:[0,1,1]
	v_pk_fma_f32 v[0:1], v[76:77], v[52:53], v[0:1] op_sel_hi:[0,1,1]
	v_pk_fma_f32 v[2:3], v[68:69], v[14:15], v[2:3] op_sel_hi:[0,1,1]
	v_max3_f32 v4, v4, v56, v57
	s_waitcnt lgkmcnt(2)
	v_pk_fma_f32 v[28:29], v[78:79], v[28:29], v[112:113] op_sel_hi:[0,1,1]
	v_pk_fma_f32 v[16:17], v[82:83], v[108:109], v[16:17] op_sel_hi:[0,1,1]
	v_pk_fma_f32 v[18:19], v[72:73], v[38:39], v[18:19] op_sel_hi:[0,1,1]
	v_pk_fma_f32 v[0:1], v[74:75], v[32:33], v[0:1] op_sel_hi:[0,1,1]
	v_pk_fma_f32 v[2:3], v[76:77], v[54:55], v[2:3] op_sel_hi:[0,1,1]
	v_max3_f32 v4, v4, v58, v59
	v_pk_fma_f32 v[30:31], v[78:79], v[30:31], v[114:115] op_sel_hi:[0,1,1]
	v_pk_fma_f32 v[16:17], v[80:81], v[60:61], v[16:17] op_sel_hi:[0,1,1]
	v_pk_fma_f32 v[18:19], v[82:83], v[110:111], v[18:19] op_sel_hi:[0,1,1]
	v_pk_fma_f32 v[0:1], v[72:73], v[40:41], v[0:1] op_sel_hi:[0,1,1]
	v_pk_fma_f32 v[2:3], v[74:75], v[34:35], v[2:3] op_sel_hi:[0,1,1]
	v_max3_f32 v4, v4, v28, v29
	s_waitcnt lgkmcnt(0)
	v_pk_fma_f32 v[16:17], v[78:79], v[104:105], v[16:17] op_sel_hi:[0,1,1]
	v_pk_fma_f32 v[18:19], v[80:81], v[62:63], v[18:19] op_sel_hi:[0,1,1]
	v_pk_fma_f32 v[0:1], v[82:83], v[44:45], v[0:1] op_sel_hi:[0,1,1]
	v_pk_fma_f32 v[2:3], v[72:73], v[42:43], v[2:3] op_sel_hi:[0,1,1]
	v_max3_f32 v4, v4, v30, v31
	v_pk_fma_f32 v[18:19], v[78:79], v[106:107], v[18:19] op_sel_hi:[0,1,1]
	v_pk_fma_f32 v[0:1], v[80:81], v[116:117], v[0:1] op_sel_hi:[0,1,1]
	v_pk_fma_f32 v[2:3], v[82:83], v[46:47], v[2:3] op_sel_hi:[0,1,1]
	v_max3_f32 v4, v4, v16, v17
	v_pk_fma_f32 v[0:1], v[78:79], v[20:21], v[0:1] op_sel_hi:[0,1,1]
	v_pk_fma_f32 v[2:3], v[80:81], v[118:119], v[2:3] op_sel_hi:[0,1,1]
	v_max3_f32 v4, v4, v18, v19
	v_pk_fma_f32 v[2:3], v[78:79], v[22:23], v[2:3] op_sel_hi:[0,1,1]
	v_max3_f32 v4, v4, v0, v1
	v_max3_f32 v4, v4, v2, v3
	s_nop 1
	v_mov_b32_dpp v5, v4 quad_perm:[1,0,3,2] row_mask:0xf bank_mask:0xf
	s_waitcnt lgkmcnt(0)
	v_max_f32_e32 v5, v5, v5
	v_max_f32_e32 v4, v4, v5
	v_sub_f32_e32 v5, v92, v4
	v_mul_f32_e32 v5, 0x3fb8aa3b, v5
	v_sub_f32_e32 v6, v93, v4
	v_exp_f32_e32 v5, v5
	v_mul_f32_e32 v6, 0x3fb8aa3b, v6
	v_sub_f32_e32 v7, v98, v4
	v_exp_f32_e32 v6, v6
	v_mul_f32_e32 v7, 0x3fb8aa3b, v7
	v_sub_f32_e32 v8, v99, v4
	v_exp_f32_e32 v7, v7
	v_mul_f32_e32 v8, 0x3fb8aa3b, v8
	v_exp_f32_e32 v8, v8
	v_add_f32_e32 v5, 0, v5
	v_add_f32_e32 v5, v5, v6
	v_sub_f32_e32 v6, v56, v4
	v_add_f32_e32 v5, v5, v7
	v_mul_f32_e32 v6, 0x3fb8aa3b, v6
	v_sub_f32_e32 v7, v57, v4
	v_add_f32_e32 v5, v5, v8
	v_exp_f32_e32 v6, v6
	v_mul_f32_e32 v7, 0x3fb8aa3b, v7
	v_sub_f32_e32 v8, v58, v4
	v_exp_f32_e32 v7, v7
	v_mul_f32_e32 v8, 0x3fb8aa3b, v8
	v_sub_f32_e32 v9, v59, v4
	v_exp_f32_e32 v8, v8
	v_mul_f32_e32 v9, 0x3fb8aa3b, v9
	v_exp_f32_e32 v9, v9
	v_add_f32_e32 v5, v5, v6
	v_sub_f32_e32 v6, v28, v4
	v_add_f32_e32 v5, v5, v7
	v_mul_f32_e32 v6, 0x3fb8aa3b, v6
	v_sub_f32_e32 v7, v29, v4
	v_add_f32_e32 v5, v5, v8
	v_exp_f32_e32 v6, v6
	v_mul_f32_e32 v7, 0x3fb8aa3b, v7
	v_sub_f32_e32 v8, v30, v4
	v_add_f32_e32 v5, v5, v9
	v_exp_f32_e32 v7, v7
	v_mul_f32_e32 v8, 0x3fb8aa3b, v8
	v_sub_f32_e32 v9, v31, v4
	v_exp_f32_e32 v8, v8
	v_mul_f32_e32 v9, 0x3fb8aa3b, v9
	v_exp_f32_e32 v9, v9
	v_add_f32_e32 v5, v5, v6
	v_sub_f32_e32 v6, v16, v4
	v_add_f32_e32 v5, v5, v7
	v_mul_f32_e32 v6, 0x3fb8aa3b, v6
	v_sub_f32_e32 v7, v17, v4
	v_add_f32_e32 v5, v5, v8
	v_exp_f32_e32 v6, v6
	v_mul_f32_e32 v7, 0x3fb8aa3b, v7
	v_sub_f32_e32 v8, v18, v4
	v_add_f32_e32 v5, v5, v9
	v_exp_f32_e32 v7, v7
	v_mul_f32_e32 v8, 0x3fb8aa3b, v8
	v_sub_f32_e32 v9, v19, v4
	v_exp_f32_e32 v8, v8
	v_mul_f32_e32 v9, 0x3fb8aa3b, v9
	v_exp_f32_e32 v9, v9
	v_add_f32_e32 v5, v5, v6
	v_sub_f32_e32 v6, v0, v4
	v_add_f32_e32 v5, v5, v7
	v_mul_f32_e32 v6, 0x3fb8aa3b, v6
	v_sub_f32_e32 v7, v1, v4
	v_add_f32_e32 v5, v5, v8
	v_exp_f32_e32 v6, v6
	v_mul_f32_e32 v7, 0x3fb8aa3b, v7
	v_sub_f32_e32 v8, v2, v4
	v_add_f32_e32 v5, v5, v9
	v_exp_f32_e32 v7, v7
	v_mul_f32_e32 v8, 0x3fb8aa3b, v8
	v_sub_f32_e32 v9, v3, v4
	v_exp_f32_e32 v8, v8
	v_mul_f32_e32 v9, 0x3fb8aa3b, v9
	v_exp_f32_e32 v9, v9
	v_add_f32_e32 v5, v5, v6
	v_add_f32_e32 v5, v5, v7
	v_add_f32_e32 v5, v5, v8
	v_add_f32_e32 v5, v5, v9
	s_nop 1
	v_mov_b32_dpp v6, v5 quad_perm:[1,0,3,2] row_mask:0xf bank_mask:0xf
	s_and_b64 exec, exec, s[8:9]
	s_cbranch_execz .LBB2_371
	s_waitcnt lgkmcnt(0)
	v_add_f32_e32 v5, v5, v6
	s_mov_b32 s0, 0x800000
	v_cmp_gt_f32_e32 vcc, s0, v5
	s_mov_b32 s0, 0x3f317217
	v_mov_b32_e32 v67, 0
	v_cndmask_b32_e64 v6, 0, 32, vcc
	v_ldexp_f32 v5, v5, v6
	v_log_f32_e32 v5, v5
	s_nop 0
	v_mul_f32_e32 v6, 0x3f317217, v5
	v_fma_f32 v6, v5, s0, -v6
	v_fmamk_f32 v6, v5, 0x3377d1cf, v6
	s_mov_b32 s0, 0x7f800000
	v_fmac_f32_e32 v6, 0x3f317217, v5
	v_cmp_lt_f32_e64 s[0:1], |v5|, s0
	s_nop 1
	v_cndmask_b32_e64 v5, v5, v6, s[0:1]
	v_mov_b32_e32 v6, 0x41b17218
	v_cndmask_b32_e32 v6, 0, v6, vcc
	v_sub_f32_e32 v5, v5, v6
	v_add_f32_e32 v10, v4, v5
	s_mov_b64 s[0:1], exec
	s_bcnt1_i32_b64 s94, exec
	s_mulk_i32 s94, 0x50
	s_lshl_b32 s92, s91, 5
	s_add_i32 s92, s92, s64
	s_mulk_i32 s92, 0xa0
	s_add_u32 s92, s52, s92
	s_addc_u32 s93, s53, 0
	s_mul_i32 s95, s91, 0x1400
	s_add_i32 s90, s95, 0x11940
	s_add_i32 s95, s95, 0x10000
	s_cmp_lt_u32 s91, 5
	s_cselect_b32 s95, s95, s90
	v_mbcnt_lo_u32_b32 v9, -1, 0
	v_mbcnt_hi_u32_b32 v9, -1, v9
	v_mul_u32_u24_e32 v8, 0x50, v9
	v_add_u32_e32 v8, s95, v8
	v_sub_f32_e32 v7, v99, v10
	v_sub_f32_e32 v6, v98, v10
	v_sub_f32_e32 v5, v93, v10
	v_sub_f32_e32 v4, v92, v10
	ds_write_b128 v8, v[4:7]
	v_sub_f32_e32 v3, v3, v10
	v_sub_f32_e32 v2, v2, v10
	v_sub_f32_e32 v7, v59, v10
	v_sub_f32_e32 v6, v58, v10
	v_sub_f32_e32 v5, v57, v10
	v_sub_f32_e32 v4, v56, v10
	ds_write_b128 v8, v[4:7] offset:16
	v_sub_f32_e32 v1, v1, v10
	v_sub_f32_e32 v0, v0, v10
	v_sub_f32_e32 v7, v31, v10
	v_sub_f32_e32 v6, v30, v10
	v_sub_f32_e32 v5, v29, v10
	v_sub_f32_e32 v4, v28, v10
	ds_write_b128 v8, v[4:7] offset:32
	ds_write_b128 v8, v[0:3] offset:64
	v_sub_f32_e32 v7, v19, v10
	v_sub_f32_e32 v6, v18, v10
	v_sub_f32_e32 v5, v17, v10
	v_sub_f32_e32 v4, v16, v10
	ds_write_b128 v8, v[4:7] offset:48
	s_mov_b64 exec, -1
	v_mbcnt_lo_u32_b32 v9, -1, 0
	v_mbcnt_hi_u32_b32 v9, -1, v9
	v_lshlrev_b32_e32 v9, 4, v9
	v_add_u32_e32 v8, s95, v9
	v_add_u32_e32 v11, 0x1000, v9
	s_waitcnt lgkmcnt(0)
	ds_read_b128 v[12:15], v8
	ds_read_b128 v[16:19], v8 offset:1024
	ds_read_b128 v[20:23], v8 offset:2048
	ds_read_b128 v[24:27], v8 offset:3072
	ds_read_b128 v[28:31], v8 offset:4096
	v_cmp_gt_i32_e32 vcc, s94, v9
	s_mov_b64 exec, vcc
	s_waitcnt lgkmcnt(4)
	global_store_dwordx4 v9, v[12:15], s[92:93] sc0 sc1
	s_sub_i32 s94, s94, 0x400
	v_cmp_gt_i32_e32 vcc, s94, v9
	s_mov_b64 exec, vcc
	s_waitcnt lgkmcnt(3)
	global_store_dwordx4 v9, v[16:19], s[92:93] offset:1024 sc0 sc1
	s_sub_i32 s94, s94, 0x400
	v_cmp_gt_i32_e32 vcc, s94, v9
	s_mov_b64 exec, vcc
	s_waitcnt lgkmcnt(2)
	global_store_dwordx4 v9, v[20:23], s[92:93] offset:2048 sc0 sc1
	s_sub_i32 s94, s94, 0x400
	v_cmp_gt_i32_e32 vcc, s94, v9
	s_mov_b64 exec, vcc
	s_waitcnt lgkmcnt(1)
	global_store_dwordx4 v9, v[24:27], s[92:93] offset:3072 sc0 sc1
	s_sub_i32 s94, s94, 0x400
	v_cmp_gt_i32_e32 vcc, s94, v9
	s_mov_b64 exec, vcc
	s_waitcnt lgkmcnt(0)
	global_store_dwordx4 v11, v[28:31], s[92:93] sc0 sc1
